# baseline (speedup 1.0000x reference)
.LBB1_23:
	s_or_b64 exec, exec, s[0:1]
	v_mov_b32_e32 v2, 0x24400
	s_movk_i32 s0, 0x80
	v_lshl_add_u32 v167, v172, 2, v2
	v_cmp_gt_u32_e32 vcc, s0, v0
	s_waitcnt lgkmcnt(0)
	s_barrier
	s_and_saveexec_b64 s[0:1], vcc
	s_cbranch_execz .LBB1_25
	v_cmp_gt_u32_e32 vcc, 64, v0
	s_movk_i32 s3, 0x190
	s_nop 0
	v_cndmask_b32_e32 v2, v166, v165, vcc
	v_mad_u32_u24 v18, v67, s3, v2
	ds_read_b128 v[176:179], v18
	ds_read_b128 v[180:183], v18 offset:16
	ds_read_b128 v[184:187], v18 offset:32
	ds_read_b128 v[188:191], v18 offset:48
	ds_read_b128 v[192:195], v18 offset:64
	ds_read_b128 v[196:199], v18 offset:80
	ds_read_b128 v[200:203], v18 offset:96
	ds_read_b128 v[204:207], v18 offset:112
	ds_read_b128 v[208:211], v18 offset:128
	ds_read_b128 v[212:215], v18 offset:144
	ds_read_b128 v[216:219], v18 offset:160
	ds_read_b128 v[220:223], v18 offset:176
	s_mov_b32 s3, 0x800000
	s_waitcnt lgkmcnt(11)
	v_pk_mul_f32 v[2:3], v[176:177], v[176:177]
	v_pk_fma_f32 v[2:3], v[178:179], v[178:179], v[2:3]
	ds_read_b128 v[176:179], v18 offset:192
	s_waitcnt lgkmcnt(11)
	v_pk_fma_f32 v[2:3], v[180:181], v[180:181], v[2:3]
	v_pk_fma_f32 v[2:3], v[182:183], v[182:183], v[2:3]
	ds_read_b128 v[180:183], v18 offset:208
	s_waitcnt lgkmcnt(11)
	v_pk_fma_f32 v[2:3], v[184:185], v[184:185], v[2:3]
	v_pk_fma_f32 v[2:3], v[186:187], v[186:187], v[2:3]
	ds_read_b128 v[184:187], v18 offset:224
	s_waitcnt lgkmcnt(11)
	v_pk_fma_f32 v[2:3], v[188:189], v[188:189], v[2:3]
	v_pk_fma_f32 v[2:3], v[190:191], v[190:191], v[2:3]
	ds_read_b128 v[188:191], v18 offset:240
	s_waitcnt lgkmcnt(11)
	v_pk_fma_f32 v[2:3], v[192:193], v[192:193], v[2:3]
	v_pk_fma_f32 v[2:3], v[194:195], v[194:195], v[2:3]
	ds_read_b128 v[192:195], v18 offset:256
	s_waitcnt lgkmcnt(11)
	v_pk_fma_f32 v[2:3], v[196:197], v[196:197], v[2:3]
	v_pk_fma_f32 v[2:3], v[198:199], v[198:199], v[2:3]
	ds_read_b128 v[196:199], v18 offset:272
	s_waitcnt lgkmcnt(11)
	v_pk_fma_f32 v[2:3], v[200:201], v[200:201], v[2:3]
	v_pk_fma_f32 v[2:3], v[202:203], v[202:203], v[2:3]
	ds_read_b128 v[200:203], v18 offset:288
	s_waitcnt lgkmcnt(11)
	v_pk_fma_f32 v[2:3], v[204:205], v[204:205], v[2:3]
	v_pk_fma_f32 v[2:3], v[206:207], v[206:207], v[2:3]
	ds_read_b128 v[204:207], v18 offset:304
	s_waitcnt lgkmcnt(11)
	v_pk_fma_f32 v[2:3], v[208:209], v[208:209], v[2:3]
	v_pk_fma_f32 v[2:3], v[210:211], v[210:211], v[2:3]
	ds_read_b128 v[208:211], v18 offset:320
	s_waitcnt lgkmcnt(11)
	v_pk_fma_f32 v[2:3], v[212:213], v[212:213], v[2:3]
	v_pk_fma_f32 v[2:3], v[214:215], v[214:215], v[2:3]
	ds_read_b128 v[212:215], v18 offset:336
	s_waitcnt lgkmcnt(11)
	v_pk_fma_f32 v[2:3], v[216:217], v[216:217], v[2:3]
	v_pk_fma_f32 v[2:3], v[218:219], v[218:219], v[2:3]
	ds_read_b128 v[216:219], v18 offset:352
	s_waitcnt lgkmcnt(11)
	v_pk_fma_f32 v[2:3], v[220:221], v[220:221], v[2:3]
	v_pk_fma_f32 v[2:3], v[222:223], v[222:223], v[2:3]
	ds_read_b128 v[220:223], v18 offset:368
	s_waitcnt lgkmcnt(11)
	v_pk_fma_f32 v[2:3], v[176:177], v[176:177], v[2:3]
	v_pk_fma_f32 v[2:3], v[178:179], v[178:179], v[2:3]
	s_waitcnt lgkmcnt(10)
	v_pk_fma_f32 v[2:3], v[180:181], v[180:181], v[2:3]
	v_pk_fma_f32 v[2:3], v[182:183], v[182:183], v[2:3]
	s_waitcnt lgkmcnt(9)
	v_pk_fma_f32 v[2:3], v[184:185], v[184:185], v[2:3]
	v_pk_fma_f32 v[2:3], v[186:187], v[186:187], v[2:3]
	s_waitcnt lgkmcnt(8)
	v_pk_fma_f32 v[2:3], v[188:189], v[188:189], v[2:3]
	v_pk_fma_f32 v[2:3], v[190:191], v[190:191], v[2:3]
	s_waitcnt lgkmcnt(7)
	v_pk_fma_f32 v[2:3], v[192:193], v[192:193], v[2:3]
	v_pk_fma_f32 v[2:3], v[194:195], v[194:195], v[2:3]
	s_waitcnt lgkmcnt(6)
	v_pk_fma_f32 v[2:3], v[196:197], v[196:197], v[2:3]
	v_pk_fma_f32 v[2:3], v[198:199], v[198:199], v[2:3]
	s_waitcnt lgkmcnt(5)
	v_pk_fma_f32 v[2:3], v[200:201], v[200:201], v[2:3]
	v_pk_fma_f32 v[2:3], v[202:203], v[202:203], v[2:3]
	s_waitcnt lgkmcnt(4)
	v_pk_fma_f32 v[2:3], v[204:205], v[204:205], v[2:3]
	v_pk_fma_f32 v[2:3], v[206:207], v[206:207], v[2:3]
	s_waitcnt lgkmcnt(3)
	v_pk_fma_f32 v[2:3], v[208:209], v[208:209], v[2:3]
	v_pk_fma_f32 v[2:3], v[210:211], v[210:211], v[2:3]
	s_waitcnt lgkmcnt(2)
	v_pk_fma_f32 v[2:3], v[212:213], v[212:213], v[2:3]
	v_pk_fma_f32 v[2:3], v[214:215], v[214:215], v[2:3]
	s_waitcnt lgkmcnt(1)
	v_pk_fma_f32 v[2:3], v[216:217], v[216:217], v[2:3]
	v_pk_fma_f32 v[2:3], v[218:219], v[218:219], v[2:3]
	s_waitcnt lgkmcnt(0)
	v_pk_fma_f32 v[2:3], v[220:221], v[220:221], v[2:3]
	v_pk_fma_f32 v[2:3], v[222:223], v[222:223], v[2:3]
	s_nop 0
	v_add_f32_e32 v2, v2, v3
	v_add_f32_e32 v2, 0x358637bd, v2
	v_mul_f32_e32 v3, 0x4b800000, v2
	v_cmp_gt_f32_e32 vcc, s3, v2
	s_nop 1
	v_cndmask_b32_e32 v2, v2, v3, vcc
	v_rsq_f32_e32 v2, v2
	s_nop 0
	v_mul_f32_e32 v3, 0x45800000, v2
	v_cndmask_b32_e32 v2, v2, v3, vcc
	v_lshl_add_u32 v3, v0, 2, v167
	ds_write_b32 v3, v2
